# speedup vs baseline: 1.0015x; 1.0015x over previous
_Z11center_mainPKfPKcS0_Pf:
	s_load_dwordx4 s[4:7], s[0:1], 0x0
	s_load_dwordx4 s[8:11], s[0:1], 0x10
	s_and_b32 s3, s2, 7
	s_lshr_b32 s12, s2, 3
	s_mov_b32 s30, s2
	v_lshrrev_b32_e32 v1, 6, v0
	v_and_b32_e32 v2, 63, v0
	v_bfe_u32 v3, v0, 3, 3
	v_and_b32_e32 v4, 7, v0
	v_lshrrev_b32_e32 v5, 7, v0
	v_bfe_u32 v6, v0, 6, 1
	v_lshl_or_b32 v7, v5, 3, v3
	v_lshlrev_b32_e32 v8, 10, v7
	v_lshl_or_b32 v8, v6, 9, v8
	v_lshl_or_b32 v226, v4, 4, v8
	v_lshlrev_b32_e32 v17, 15, v1
	v_lshl_or_b32 v227, v2, 5, v17
	v_lshlrev_b32_e32 v237, 3, v0
	s_lshl_b32 s13, s3, 22
	s_lshl_b32 s14, s12, 15
	s_add_u32 s13, s13, s14
	s_lshl_b32 s15, s3, 18
	s_lshl_b32 s28, s3, 12
	s_waitcnt lgkmcnt(0)
	s_add_u32 s16, s4, s13
	s_addc_u32 s17, s5, 0
	global_load_dwordx4 v[194:197], v226, s[16:17] offset:0 nt
	global_load_dwordx4 v[198:201], v226, s[16:17] offset:128 nt
	global_load_dwordx4 v[202:205], v226, s[16:17] offset:256 nt
	global_load_dwordx4 v[206:209], v226, s[16:17] offset:384 nt
	s_add_u32 s8, s8, s28
	s_addc_u32 s9, s9, 0
	global_load_dwordx2 v[238:239], v237, s[8:9]
	s_add_u32 s24, s6, s15
	s_addc_u32 s25, s7, 0
	s_add_u32 s32, s24, 0x1000
	s_addc_u32 s33, s25, 0
	s_add_u32 s34, s24, 0x2000
	s_addc_u32 s35, s25, 0
	s_add_u32 s36, s24, 0x3000
	s_addc_u32 s37, s25, 0
	s_add_u32 s38, s24, 0x4000
	s_addc_u32 s39, s25, 0
	s_add_u32 s40, s24, 0x5000
	s_addc_u32 s41, s25, 0
	s_add_u32 s42, s24, 0x6000
	s_addc_u32 s43, s25, 0
	s_add_u32 s44, s24, 0x7000
	s_addc_u32 s45, s25, 0
	global_load_dwordx4 v[34:37], v227, s[24:25] offset:0
	global_load_dwordx4 v[38:41], v227, s[24:25] offset:16
	global_load_dwordx4 v[26:29], v227, s[24:25] offset:2048
	global_load_dwordx4 v[30:33], v227, s[24:25] offset:2064
	global_load_dwordx4 v[50:53], v227, s[32:33] offset:0
	global_load_dwordx4 v[54:57], v227, s[32:33] offset:16
	global_load_dwordx4 v[42:45], v227, s[32:33] offset:2048
	global_load_dwordx4 v[46:49], v227, s[32:33] offset:2064
	global_load_dwordx4 v[18:21], v227, s[34:35] offset:0
	global_load_dwordx4 v[22:25], v227, s[34:35] offset:16
	global_load_dwordx4 v[130:133], v227, s[34:35] offset:2048
	global_load_dwordx4 v[134:137], v227, s[34:35] offset:2064
	global_load_dwordx4 v[122:125], v227, s[36:37] offset:0
	global_load_dwordx4 v[126:129], v227, s[36:37] offset:16
	global_load_dwordx4 v[138:141], v227, s[36:37] offset:2048
	global_load_dwordx4 v[142:145], v227, s[36:37] offset:2064
	global_load_dwordx4 v[98:101], v227, s[38:39] offset:0
	global_load_dwordx4 v[102:105], v227, s[38:39] offset:16
	global_load_dwordx4 v[90:93], v227, s[38:39] offset:2048
	global_load_dwordx4 v[94:97], v227, s[38:39] offset:2064
	global_load_dwordx4 v[114:117], v227, s[40:41] offset:0
	global_load_dwordx4 v[118:121], v227, s[40:41] offset:16
	global_load_dwordx4 v[106:109], v227, s[40:41] offset:2048
	global_load_dwordx4 v[110:113], v227, s[40:41] offset:2064
	global_load_dwordx4 v[58:61], v227, s[42:43] offset:0
	global_load_dwordx4 v[62:65], v227, s[42:43] offset:16
	global_load_dwordx4 v[66:69], v227, s[42:43] offset:2048
	global_load_dwordx4 v[70:73], v227, s[42:43] offset:2064
	global_load_dwordx4 v[74:77], v227, s[44:45] offset:0
	global_load_dwordx4 v[78:81], v227, s[44:45] offset:16
	global_load_dwordx4 v[82:85], v227, s[44:45] offset:2048
	global_load_dwordx4 v[86:89], v227, s[44:45] offset:2064
	s_add_u32 s18, s16, 0x100000
	s_addc_u32 s19, s17, 0
	s_add_u32 s20, s16, 0x200000
	s_addc_u32 s21, s17, 0
	s_add_u32 s22, s16, 0x300000
	s_addc_u32 s23, s17, 0
	v_mul_u32_u24_e32 v9, 0x110, v7
	v_lshl_add_u32 v9, v6, 7, v9
	v_lshl_add_u32 v228, v4, 4, v9
	v_lshlrev_b32_e32 v10, 6, v7
	v_lshl_or_b32 v10, v6, 5, v10
	v_lshl_or_b32 v229, v4, 2, v10
	v_and_b32_e32 v11, 31, v0
	v_bfe_u32 v12, v0, 5, 1
	v_mul_u32_u24_e32 v13, 0x110, v11
	v_lshl_add_u32 v230, v12, 5, v13
	v_lshlrev_b32_e32 v14, 9, v1
	v_lshl_or_b32 v231, v12, 4, v14
	v_xor_b32_e32 v15, 32, v2
	v_lshlrev_b32_e32 v232, 2, v15
	v_xor_b32_e32 v15, 16, v2
	v_lshlrev_b32_e32 v247, 2, v15
	v_lshlrev_b32_e32 v16, 7, v1
	v_lshl_or_b32 v233, v11, 2, v16
	v_mov_b32_e32 v234, 0x7f7f7f7f
	s_waitcnt vmcnt(32)
	ds_write_b64 v237, v[238:239] offset:34816
	v_mul_f32_e32 v244, v194, v194
	v_mul_f32_e32 v245, v198, v198
	v_cvt_pk_fp8_f32 v240, v194, v195
	v_cvt_pk_fp8_f32 v241, v198, v199
	v_cvt_pk_fp8_f32 v242, v202, v203
	v_cvt_pk_fp8_f32 v243, v206, v207
	v_fmac_f32_e32 v244, v195, v195
	v_fmac_f32_e32 v245, v199, v199
	v_fmac_f32_e32 v244, v196, v196
	v_fmac_f32_e32 v245, v200, v200
	v_fmac_f32_e32 v244, v197, v197
	v_fmac_f32_e32 v245, v201, v201
	v_fmac_f32_e32 v244, v202, v202
	v_fmac_f32_e32 v245, v206, v206
	v_fmac_f32_e32 v244, v203, v203
	v_fmac_f32_e32 v245, v207, v207
	v_fmac_f32_e32 v244, v204, v204
	v_fmac_f32_e32 v245, v208, v208
	v_fmac_f32_e32 v244, v205, v205
	v_fmac_f32_e32 v245, v209, v209
	v_cvt_pk_fp8_f32 v240, v196, v197 op_sel:[0,0,1]
	v_cvt_pk_fp8_f32 v241, v200, v201 op_sel:[0,0,1]
	v_cvt_pk_fp8_f32 v242, v204, v205 op_sel:[0,0,1]
	v_cvt_pk_fp8_f32 v243, v208, v209 op_sel:[0,0,1]
	v_add_f32_e32 v244, v244, v245
	s_nop 0
	ds_write_b128 v228, v[240:243] offset:0
	ds_write_b32 v229, v244 offset:38912
	global_load_dwordx4 v[210:213], v226, s[18:19] offset:0 nt
	global_load_dwordx4 v[214:217], v226, s[18:19] offset:128 nt
	global_load_dwordx4 v[218:221], v226, s[18:19] offset:256 nt
	global_load_dwordx4 v[222:225], v226, s[18:19] offset:384 nt
	s_waitcnt lgkmcnt(0)
	s_barrier
	ds_read_b128 v[162:165], v230 offset:0
	ds_read_b128 v[166:169], v230 offset:16
	ds_read_b128 v[2:5], v231 offset:34816
	ds_read_b128 v[6:9], v231 offset:34848
	ds_read_b128 v[10:13], v231 offset:34880
	ds_read_b128 v[14:17], v231 offset:34912
	ds_read_b128 v[170:173], v230 offset:64
	ds_read_b128 v[174:177], v230 offset:80
	ds_read_b128 v[178:181], v230 offset:128
	ds_read_b128 v[182:185], v230 offset:144
	ds_read_b128 v[186:189], v230 offset:192
	ds_read_b128 v[190:193], v230 offset:208
	s_waitcnt vmcnt(34) lgkmcnt(6)
	v_mfma_f32_32x32x64_f8f6f4 v[2:17], v[34:41], v[162:169], v[2:17]
	s_waitcnt vmcnt(32) lgkmcnt(4)
	v_mfma_f32_32x32x64_f8f6f4 v[2:17], v[26:33], v[170:177], v[2:17]
	ds_read_b128 v[146:149], v231 offset:34944
	ds_read_b128 v[150:153], v231 offset:34976
	ds_read_b128 v[154:157], v231 offset:35008
	ds_read_b128 v[158:161], v231 offset:35040
	s_waitcnt vmcnt(30) lgkmcnt(6)
	v_mfma_f32_32x32x64_f8f6f4 v[2:17], v[50:57], v[178:185], v[2:17]
	s_waitcnt vmcnt(28) lgkmcnt(4)
	v_mfma_f32_32x32x64_f8f6f4 v[2:17], v[42:49], v[186:193], v[2:17]
	s_waitcnt lgkmcnt(0)
	s_waitcnt vmcnt(26)
	v_mfma_f32_32x32x64_f8f6f4 v[146:161], v[18:25], v[162:169], v[146:161]
	s_waitcnt vmcnt(24)
	v_mfma_f32_32x32x64_f8f6f4 v[146:161], v[130:137], v[170:177], v[146:161]
	v_min3_f32 v2, v2, v3, v4
	v_min3_f32 v5, v5, v6, v7
	v_min3_f32 v8, v8, v9, v10
	v_min3_f32 v11, v11, v12, v13
	v_min3_f32 v14, v14, v15, v16
	v_min3_f32 v2, v2, v5, v8
	v_min3_f32 v11, v11, v14, v17
	v_min_f32_e32 v235, v2, v11
	ds_read_b128 v[2:5], v231 offset:35072
	ds_read_b128 v[6:9], v231 offset:35104
	ds_read_b128 v[10:13], v231 offset:35136
	ds_read_b128 v[14:17], v231 offset:35168
	s_waitcnt vmcnt(22)
	v_mfma_f32_32x32x64_f8f6f4 v[146:161], v[122:129], v[178:185], v[146:161]
	s_waitcnt vmcnt(20)
	v_mfma_f32_32x32x64_f8f6f4 v[146:161], v[138:145], v[186:193], v[146:161]
	s_waitcnt vmcnt(18) lgkmcnt(0)
	v_mfma_f32_32x32x64_f8f6f4 v[2:17], v[98:105], v[162:169], v[2:17]
	s_waitcnt vmcnt(16)
	v_mfma_f32_32x32x64_f8f6f4 v[2:17], v[90:97], v[170:177], v[2:17]
	v_min3_f32 v146, v146, v147, v148
	v_min3_f32 v149, v149, v150, v151
	v_min3_f32 v152, v152, v153, v154
	v_min3_f32 v155, v155, v156, v157
	v_min3_f32 v158, v158, v159, v160
	v_min3_f32 v146, v146, v149, v152
	v_min3_f32 v155, v155, v158, v161
	v_min3_f32 v235, v235, v146, v155
	ds_read_b128 v[146:149], v231 offset:35200
	ds_read_b128 v[150:153], v231 offset:35232
	ds_read_b128 v[154:157], v231 offset:35264
	ds_read_b128 v[158:161], v231 offset:35296
	s_waitcnt vmcnt(14)
	v_mfma_f32_32x32x64_f8f6f4 v[2:17], v[114:121], v[178:185], v[2:17]
	s_waitcnt vmcnt(12)
	v_mfma_f32_32x32x64_f8f6f4 v[2:17], v[106:113], v[186:193], v[2:17]
	s_waitcnt vmcnt(10) lgkmcnt(0)
	v_mfma_f32_32x32x64_f8f6f4 v[146:161], v[58:65], v[162:169], v[146:161]
	s_waitcnt vmcnt(8)
	v_mfma_f32_32x32x64_f8f6f4 v[146:161], v[66:73], v[170:177], v[146:161]
	v_min3_f32 v2, v2, v3, v4
	v_min3_f32 v5, v5, v6, v7
	v_min3_f32 v8, v8, v9, v10
	v_min3_f32 v11, v11, v12, v13
	v_min3_f32 v14, v14, v15, v16
	v_min3_f32 v2, v2, v5, v8
	v_min3_f32 v11, v11, v14, v17
	v_min3_f32 v235, v235, v2, v11
	ds_read_b128 v[2:5], v231 offset:34816
	ds_read_b128 v[6:9], v231 offset:34848
	ds_read_b128 v[10:13], v231 offset:34880
	ds_read_b128 v[14:17], v231 offset:34912
	s_waitcnt vmcnt(6)
	v_mfma_f32_32x32x64_f8f6f4 v[146:161], v[74:81], v[178:185], v[146:161]
	s_waitcnt vmcnt(4)
	v_mfma_f32_32x32x64_f8f6f4 v[146:161], v[82:89], v[186:193], v[146:161]
	s_waitcnt vmcnt(0)
	v_mul_f32_e32 v244, v210, v210
	v_mul_f32_e32 v245, v214, v214
	v_cvt_pk_fp8_f32 v240, v210, v211
	v_cvt_pk_fp8_f32 v241, v214, v215
	v_cvt_pk_fp8_f32 v242, v218, v219
	v_cvt_pk_fp8_f32 v243, v222, v223
	v_fmac_f32_e32 v244, v211, v211
	v_fmac_f32_e32 v245, v215, v215
	v_fmac_f32_e32 v244, v212, v212
	v_fmac_f32_e32 v245, v216, v216
	v_fmac_f32_e32 v244, v213, v213
	v_fmac_f32_e32 v245, v217, v217
	v_fmac_f32_e32 v244, v218, v218
	v_fmac_f32_e32 v245, v222, v222
	v_fmac_f32_e32 v244, v219, v219
	v_fmac_f32_e32 v245, v223, v223
	v_fmac_f32_e32 v244, v220, v220
	v_fmac_f32_e32 v245, v224, v224
	v_fmac_f32_e32 v244, v221, v221
	v_fmac_f32_e32 v245, v225, v225
	v_cvt_pk_fp8_f32 v240, v212, v213 op_sel:[0,0,1]
	v_cvt_pk_fp8_f32 v241, v216, v217 op_sel:[0,0,1]
	v_cvt_pk_fp8_f32 v242, v220, v221 op_sel:[0,0,1]
	v_cvt_pk_fp8_f32 v243, v224, v225 op_sel:[0,0,1]
	v_add_f32_e32 v244, v244, v245
	s_nop 0
	ds_write_b128 v228, v[240:243] offset:8704
	ds_write_b32 v229, v244 offset:40960
	global_load_dwordx4 v[194:197], v226, s[20:21] offset:0 nt
	global_load_dwordx4 v[198:201], v226, s[20:21] offset:128 nt
	global_load_dwordx4 v[202:205], v226, s[20:21] offset:256 nt
	global_load_dwordx4 v[206:209], v226, s[20:21] offset:384 nt
	s_waitcnt lgkmcnt(0)
	s_barrier
	ds_read_b128 v[162:165], v230 offset:8704
	ds_read_b128 v[166:169], v230 offset:8720
	ds_read_b128 v[170:173], v230 offset:8768
	ds_read_b128 v[174:177], v230 offset:8784
	ds_read_b128 v[178:181], v230 offset:8832
	ds_read_b128 v[182:185], v230 offset:8848
	ds_read_b128 v[186:189], v230 offset:8896
	ds_read_b128 v[190:193], v230 offset:8912
	s_waitcnt lgkmcnt(6)
	v_mfma_f32_32x32x64_f8f6f4 v[2:17], v[34:41], v[162:169], v[2:17]
	s_waitcnt lgkmcnt(4)
	v_mfma_f32_32x32x64_f8f6f4 v[2:17], v[26:33], v[170:177], v[2:17]
	v_min3_f32 v146, v146, v147, v148
	v_min3_f32 v149, v149, v150, v151
	v_min3_f32 v152, v152, v153, v154
	v_min3_f32 v155, v155, v156, v157
	v_min3_f32 v158, v158, v159, v160
	v_min3_f32 v146, v146, v149, v152
	v_min3_f32 v155, v155, v158, v161
	v_min3_f32 v235, v235, v146, v155
	ds_bpermute_b32 v246, v232, v235
	ds_read_b128 v[146:149], v231 offset:34944
	ds_read_b128 v[150:153], v231 offset:34976
	ds_read_b128 v[154:157], v231 offset:35008
	ds_read_b128 v[158:161], v231 offset:35040
	s_waitcnt lgkmcnt(7)
	v_mfma_f32_32x32x64_f8f6f4 v[2:17], v[50:57], v[178:185], v[2:17]
	s_waitcnt lgkmcnt(5)
	v_mfma_f32_32x32x64_f8f6f4 v[2:17], v[42:49], v[186:193], v[2:17]
	s_waitcnt lgkmcnt(0)
	v_min_f32_e32 v246, v235, v246
	ds_write_b32 v233, v246 offset:47104
	v_mfma_f32_32x32x64_f8f6f4 v[146:161], v[18:25], v[162:169], v[146:161]
	v_mfma_f32_32x32x64_f8f6f4 v[146:161], v[130:137], v[170:177], v[146:161]
	v_min3_f32 v2, v2, v3, v4
	v_min3_f32 v5, v5, v6, v7
	v_min3_f32 v8, v8, v9, v10
	v_min3_f32 v11, v11, v12, v13
	v_min3_f32 v14, v14, v15, v16
	v_min3_f32 v2, v2, v5, v8
	v_min3_f32 v11, v11, v14, v17
	v_min_f32_e32 v236, v2, v11
	ds_read_b128 v[2:5], v231 offset:35072
	ds_read_b128 v[6:9], v231 offset:35104
	ds_read_b128 v[10:13], v231 offset:35136
	ds_read_b128 v[14:17], v231 offset:35168
	v_mfma_f32_32x32x64_f8f6f4 v[146:161], v[122:129], v[178:185], v[146:161]
	v_mfma_f32_32x32x64_f8f6f4 v[146:161], v[138:145], v[186:193], v[146:161]
	s_waitcnt lgkmcnt(0)
	v_mfma_f32_32x32x64_f8f6f4 v[2:17], v[98:105], v[162:169], v[2:17]
	v_mfma_f32_32x32x64_f8f6f4 v[2:17], v[90:97], v[170:177], v[2:17]
	v_min3_f32 v146, v146, v147, v148
	v_min3_f32 v149, v149, v150, v151
	v_min3_f32 v152, v152, v153, v154
	v_min3_f32 v155, v155, v156, v157
	v_min3_f32 v158, v158, v159, v160
	v_min3_f32 v146, v146, v149, v152
	v_min3_f32 v155, v155, v158, v161
	v_min3_f32 v236, v236, v146, v155
	ds_read_b128 v[146:149], v231 offset:35200
	ds_read_b128 v[150:153], v231 offset:35232
	ds_read_b128 v[154:157], v231 offset:35264
	ds_read_b128 v[158:161], v231 offset:35296
	v_mfma_f32_32x32x64_f8f6f4 v[2:17], v[114:121], v[178:185], v[2:17]
	v_mfma_f32_32x32x64_f8f6f4 v[2:17], v[106:113], v[186:193], v[2:17]
	s_waitcnt lgkmcnt(0)
	v_mfma_f32_32x32x64_f8f6f4 v[146:161], v[58:65], v[162:169], v[146:161]
	v_mfma_f32_32x32x64_f8f6f4 v[146:161], v[66:73], v[170:177], v[146:161]
	v_min3_f32 v2, v2, v3, v4
	v_min3_f32 v5, v5, v6, v7
	v_min3_f32 v8, v8, v9, v10
	v_min3_f32 v11, v11, v12, v13
	v_min3_f32 v14, v14, v15, v16
	v_min3_f32 v2, v2, v5, v8
	v_min3_f32 v11, v11, v14, v17
	v_min3_f32 v236, v236, v2, v11
	ds_read_b128 v[2:5], v231 offset:34816
	ds_read_b128 v[6:9], v231 offset:34848
	ds_read_b128 v[10:13], v231 offset:34880
	ds_read_b128 v[14:17], v231 offset:34912
	v_mfma_f32_32x32x64_f8f6f4 v[146:161], v[74:81], v[178:185], v[146:161]
	v_mfma_f32_32x32x64_f8f6f4 v[146:161], v[82:89], v[186:193], v[146:161]
	s_waitcnt vmcnt(0)
	v_mul_f32_e32 v244, v194, v194
	v_mul_f32_e32 v245, v198, v198
	v_cvt_pk_fp8_f32 v240, v194, v195
	v_cvt_pk_fp8_f32 v241, v198, v199
	v_cvt_pk_fp8_f32 v242, v202, v203
	v_cvt_pk_fp8_f32 v243, v206, v207
	v_fmac_f32_e32 v244, v195, v195
	v_fmac_f32_e32 v245, v199, v199
	v_fmac_f32_e32 v244, v196, v196
	v_fmac_f32_e32 v245, v200, v200
	v_fmac_f32_e32 v244, v197, v197
	v_fmac_f32_e32 v245, v201, v201
	v_fmac_f32_e32 v244, v202, v202
	v_fmac_f32_e32 v245, v206, v206
	v_fmac_f32_e32 v244, v203, v203
	v_fmac_f32_e32 v245, v207, v207
	v_fmac_f32_e32 v244, v204, v204
	v_fmac_f32_e32 v245, v208, v208
	v_fmac_f32_e32 v244, v205, v205
	v_fmac_f32_e32 v245, v209, v209
	v_cvt_pk_fp8_f32 v240, v196, v197 op_sel:[0,0,1]
	v_cvt_pk_fp8_f32 v241, v200, v201 op_sel:[0,0,1]
	v_cvt_pk_fp8_f32 v242, v204, v205 op_sel:[0,0,1]
	v_cvt_pk_fp8_f32 v243, v208, v209 op_sel:[0,0,1]
	v_add_f32_e32 v244, v244, v245
	s_nop 0
	ds_write_b128 v228, v[240:243] offset:17408
	ds_write_b32 v229, v244 offset:43008
	global_load_dwordx4 v[210:213], v226, s[22:23] offset:0 nt
	global_load_dwordx4 v[214:217], v226, s[22:23] offset:128 nt
	global_load_dwordx4 v[218:221], v226, s[22:23] offset:256 nt
	global_load_dwordx4 v[222:225], v226, s[22:23] offset:384 nt
	s_waitcnt lgkmcnt(0)
	s_barrier
	ds_read_b128 v[162:165], v230 offset:17408
	ds_read_b128 v[166:169], v230 offset:17424
	ds_read_b128 v[170:173], v230 offset:17472
	ds_read_b128 v[174:177], v230 offset:17488
	ds_read_b128 v[178:181], v230 offset:17536
	ds_read_b128 v[182:185], v230 offset:17552
	ds_read_b128 v[186:189], v230 offset:17600
	ds_read_b128 v[190:193], v230 offset:17616
	s_waitcnt lgkmcnt(6)
	v_mfma_f32_32x32x64_f8f6f4 v[2:17], v[34:41], v[162:169], v[2:17]
	s_waitcnt lgkmcnt(4)
	v_mfma_f32_32x32x64_f8f6f4 v[2:17], v[26:33], v[170:177], v[2:17]
	v_min3_f32 v146, v146, v147, v148
	v_min3_f32 v149, v149, v150, v151
	v_min3_f32 v152, v152, v153, v154
	v_min3_f32 v155, v155, v156, v157
	v_min3_f32 v158, v158, v159, v160
	v_min3_f32 v146, v146, v149, v152
	v_min3_f32 v155, v155, v158, v161
	v_min3_f32 v236, v236, v146, v155
	ds_bpermute_b32 v246, v232, v236
	ds_read_b128 v[146:149], v231 offset:34944
	ds_read_b128 v[150:153], v231 offset:34976
	ds_read_b128 v[154:157], v231 offset:35008
	ds_read_b128 v[158:161], v231 offset:35040
	s_waitcnt lgkmcnt(7)
	v_mfma_f32_32x32x64_f8f6f4 v[2:17], v[50:57], v[178:185], v[2:17]
	s_waitcnt lgkmcnt(5)
	v_mfma_f32_32x32x64_f8f6f4 v[2:17], v[42:49], v[186:193], v[2:17]
	s_waitcnt lgkmcnt(0)
	v_min_f32_e32 v246, v236, v246
	ds_write_b32 v233, v246 offset:48128
	v_mfma_f32_32x32x64_f8f6f4 v[146:161], v[18:25], v[162:169], v[146:161]
	v_mfma_f32_32x32x64_f8f6f4 v[146:161], v[130:137], v[170:177], v[146:161]
	v_min3_f32 v2, v2, v3, v4
	v_min3_f32 v5, v5, v6, v7
	v_min3_f32 v8, v8, v9, v10
	v_min3_f32 v11, v11, v12, v13
	v_min3_f32 v14, v14, v15, v16
	v_min3_f32 v2, v2, v5, v8
	v_min3_f32 v11, v11, v14, v17
	v_min_f32_e32 v235, v2, v11
	ds_read_b128 v[2:5], v231 offset:35072
	ds_read_b128 v[6:9], v231 offset:35104
	ds_read_b128 v[10:13], v231 offset:35136
	ds_read_b128 v[14:17], v231 offset:35168
	v_mfma_f32_32x32x64_f8f6f4 v[146:161], v[122:129], v[178:185], v[146:161]
	v_mfma_f32_32x32x64_f8f6f4 v[146:161], v[138:145], v[186:193], v[146:161]
	s_waitcnt lgkmcnt(0)
	v_mfma_f32_32x32x64_f8f6f4 v[2:17], v[98:105], v[162:169], v[2:17]
	v_mfma_f32_32x32x64_f8f6f4 v[2:17], v[90:97], v[170:177], v[2:17]
	v_min3_f32 v146, v146, v147, v148
	v_min3_f32 v149, v149, v150, v151
	v_min3_f32 v152, v152, v153, v154
	v_min3_f32 v155, v155, v156, v157
	v_min3_f32 v158, v158, v159, v160
	v_min3_f32 v146, v146, v149, v152
	v_min3_f32 v155, v155, v158, v161
	v_min3_f32 v235, v235, v146, v155
	ds_read_b128 v[146:149], v231 offset:35200
	ds_read_b128 v[150:153], v231 offset:35232
	ds_read_b128 v[154:157], v231 offset:35264
	ds_read_b128 v[158:161], v231 offset:35296
	v_mfma_f32_32x32x64_f8f6f4 v[2:17], v[114:121], v[178:185], v[2:17]
	v_mfma_f32_32x32x64_f8f6f4 v[2:17], v[106:113], v[186:193], v[2:17]
	s_waitcnt lgkmcnt(0)
	v_mfma_f32_32x32x64_f8f6f4 v[146:161], v[58:65], v[162:169], v[146:161]
	v_mfma_f32_32x32x64_f8f6f4 v[146:161], v[66:73], v[170:177], v[146:161]
	v_min3_f32 v2, v2, v3, v4
	v_min3_f32 v5, v5, v6, v7
	v_min3_f32 v8, v8, v9, v10
	v_min3_f32 v11, v11, v12, v13
	v_min3_f32 v14, v14, v15, v16
	v_min3_f32 v2, v2, v5, v8
	v_min3_f32 v11, v11, v14, v17
	v_min3_f32 v235, v235, v2, v11
	ds_read_b128 v[2:5], v231 offset:34816
	ds_read_b128 v[6:9], v231 offset:34848
	ds_read_b128 v[10:13], v231 offset:34880
	ds_read_b128 v[14:17], v231 offset:34912
	v_mfma_f32_32x32x64_f8f6f4 v[146:161], v[74:81], v[178:185], v[146:161]
	v_mfma_f32_32x32x64_f8f6f4 v[146:161], v[82:89], v[186:193], v[146:161]
	s_waitcnt vmcnt(0)
	v_mul_f32_e32 v244, v210, v210
	v_mul_f32_e32 v245, v214, v214
	v_cvt_pk_fp8_f32 v240, v210, v211
	v_cvt_pk_fp8_f32 v241, v214, v215
	v_cvt_pk_fp8_f32 v242, v218, v219
	v_cvt_pk_fp8_f32 v243, v222, v223
	v_fmac_f32_e32 v244, v211, v211
	v_fmac_f32_e32 v245, v215, v215
	v_fmac_f32_e32 v244, v212, v212
	v_fmac_f32_e32 v245, v216, v216
	v_fmac_f32_e32 v244, v213, v213
	v_fmac_f32_e32 v245, v217, v217
	v_fmac_f32_e32 v244, v218, v218
	v_fmac_f32_e32 v245, v222, v222
	v_fmac_f32_e32 v244, v219, v219
	v_fmac_f32_e32 v245, v223, v223
	v_fmac_f32_e32 v244, v220, v220
	v_fmac_f32_e32 v245, v224, v224
	v_fmac_f32_e32 v244, v221, v221
	v_fmac_f32_e32 v245, v225, v225
	v_cvt_pk_fp8_f32 v240, v212, v213 op_sel:[0,0,1]
	v_cvt_pk_fp8_f32 v241, v216, v217 op_sel:[0,0,1]
	v_cvt_pk_fp8_f32 v242, v220, v221 op_sel:[0,0,1]
	v_cvt_pk_fp8_f32 v243, v224, v225 op_sel:[0,0,1]
	v_add_f32_e32 v244, v244, v245
	s_nop 0
	ds_write_b128 v228, v[240:243] offset:26112
	ds_write_b32 v229, v244 offset:45056
	s_waitcnt lgkmcnt(0)
	s_barrier
	ds_read_b128 v[162:165], v230 offset:26112
	ds_read_b128 v[166:169], v230 offset:26128
	ds_read_b128 v[170:173], v230 offset:26176
	ds_read_b128 v[174:177], v230 offset:26192
	ds_read_b128 v[178:181], v230 offset:26240
	ds_read_b128 v[182:185], v230 offset:26256
	ds_read_b128 v[186:189], v230 offset:26304
	ds_read_b128 v[190:193], v230 offset:26320
	s_waitcnt lgkmcnt(6)
	v_mfma_f32_32x32x64_f8f6f4 v[2:17], v[34:41], v[162:169], v[2:17]
	s_waitcnt lgkmcnt(4)
	v_mfma_f32_32x32x64_f8f6f4 v[2:17], v[26:33], v[170:177], v[2:17]
	v_min3_f32 v146, v146, v147, v148
	v_min3_f32 v149, v149, v150, v151
	v_min3_f32 v152, v152, v153, v154
	v_min3_f32 v155, v155, v156, v157
	v_min3_f32 v158, v158, v159, v160
	v_min3_f32 v146, v146, v149, v152
	v_min3_f32 v155, v155, v158, v161
	v_min3_f32 v235, v235, v146, v155
	ds_bpermute_b32 v246, v232, v235
	ds_read_b128 v[146:149], v231 offset:34944
	ds_read_b128 v[150:153], v231 offset:34976
	ds_read_b128 v[154:157], v231 offset:35008
	ds_read_b128 v[158:161], v231 offset:35040
	s_waitcnt lgkmcnt(7)
	v_mfma_f32_32x32x64_f8f6f4 v[2:17], v[50:57], v[178:185], v[2:17]
	s_waitcnt lgkmcnt(5)
	v_mfma_f32_32x32x64_f8f6f4 v[2:17], v[42:49], v[186:193], v[2:17]
	s_waitcnt lgkmcnt(0)
	v_min_f32_e32 v246, v235, v246
	ds_write_b32 v233, v246 offset:49152
	v_mfma_f32_32x32x64_f8f6f4 v[146:161], v[18:25], v[162:169], v[146:161]
	v_mfma_f32_32x32x64_f8f6f4 v[146:161], v[130:137], v[170:177], v[146:161]
	v_min3_f32 v2, v2, v3, v4
	v_min3_f32 v5, v5, v6, v7
	v_min3_f32 v8, v8, v9, v10
	v_min3_f32 v11, v11, v12, v13
	v_min3_f32 v14, v14, v15, v16
	v_min3_f32 v2, v2, v5, v8
	v_min3_f32 v11, v11, v14, v17
	v_min_f32_e32 v236, v2, v11
	ds_read_b128 v[2:5], v231 offset:35072
	ds_read_b128 v[6:9], v231 offset:35104
	ds_read_b128 v[10:13], v231 offset:35136
	ds_read_b128 v[14:17], v231 offset:35168
	v_mfma_f32_32x32x64_f8f6f4 v[146:161], v[122:129], v[178:185], v[146:161]
	v_mfma_f32_32x32x64_f8f6f4 v[146:161], v[138:145], v[186:193], v[146:161]
	s_waitcnt lgkmcnt(0)
	v_mfma_f32_32x32x64_f8f6f4 v[2:17], v[98:105], v[162:169], v[2:17]
	v_mfma_f32_32x32x64_f8f6f4 v[2:17], v[90:97], v[170:177], v[2:17]
	v_min3_f32 v146, v146, v147, v148
	v_min3_f32 v149, v149, v150, v151
	v_min3_f32 v152, v152, v153, v154
	v_min3_f32 v155, v155, v156, v157
	v_min3_f32 v158, v158, v159, v160
	v_min3_f32 v146, v146, v149, v152
	v_min3_f32 v155, v155, v158, v161
	v_min3_f32 v236, v236, v146, v155
	ds_read_b128 v[146:149], v231 offset:35200
	ds_read_b128 v[150:153], v231 offset:35232
	ds_read_b128 v[154:157], v231 offset:35264
	ds_read_b128 v[158:161], v231 offset:35296
	v_mfma_f32_32x32x64_f8f6f4 v[2:17], v[114:121], v[178:185], v[2:17]
	v_mfma_f32_32x32x64_f8f6f4 v[2:17], v[106:113], v[186:193], v[2:17]
	s_waitcnt lgkmcnt(0)
	v_mfma_f32_32x32x64_f8f6f4 v[146:161], v[58:65], v[162:169], v[146:161]
	v_mfma_f32_32x32x64_f8f6f4 v[146:161], v[66:73], v[170:177], v[146:161]
	v_min3_f32 v2, v2, v3, v4
	v_min3_f32 v5, v5, v6, v7
	v_min3_f32 v8, v8, v9, v10
	v_min3_f32 v11, v11, v12, v13
	v_min3_f32 v14, v14, v15, v16
	v_min3_f32 v2, v2, v5, v8
	v_min3_f32 v11, v11, v14, v17
	v_min3_f32 v236, v236, v2, v11
	v_mfma_f32_32x32x64_f8f6f4 v[146:161], v[74:81], v[178:185], v[146:161]
	v_mfma_f32_32x32x64_f8f6f4 v[146:161], v[82:89], v[186:193], v[146:161]
	v_cmp_gt_u32_e32 vcc, 0x80, v0
	s_and_saveexec_b64 s[34:35], vcc
	v_lshlrev_b32_e32 v36, 6, v0
	ds_read_b128 v[20:23], v36 offset:38912
	ds_read_b128 v[24:27], v36 offset:38928
	ds_read_b128 v[28:31], v36 offset:38944
	ds_read_b128 v[32:35], v36 offset:38960
	s_mov_b64 exec, s[34:35]
	s_nop 15
	s_nop 3
	v_min3_f32 v146, v146, v147, v148
	v_min3_f32 v149, v149, v150, v151
	v_min3_f32 v152, v152, v153, v154
	v_min3_f32 v155, v155, v156, v157
	v_min3_f32 v158, v158, v159, v160
	v_min3_f32 v146, v146, v149, v152
	v_min3_f32 v155, v155, v158, v161
	v_min3_f32 v236, v236, v146, v155
	ds_bpermute_b32 v246, v232, v236
	s_waitcnt lgkmcnt(0)
	v_min_f32_e32 v246, v236, v246
	ds_write_b32 v233, v246 offset:50176
	s_waitcnt lgkmcnt(0)
	s_barrier
	v_readfirstlane_b32 s2, v1
	s_nop 3
	s_cmp_gt_u32 s2, 1
	s_cbranch_scc1 .Lmain_end
	v_and_b32_e32 v2, 31, v0
	v_lshlrev_b32_e32 v3, 5, v0
	v_and_b32_e32 v3, 0xc00, v3
	v_lshl_or_b32 v8, v2, 2, v3
	v_add_u32_e32 v8, 0xb800, v8
	ds_read2_b32 v[2:3], v8 offset1:32
	ds_read2_b32 v[4:5], v8 offset0:64 offset1:96
	ds_read2_b32 v[6:7], v8 offset0:128 offset1:160
	ds_read2_b32 v[10:11], v8 offset0:192 offset1:224
	s_mov_b32 s8, 0xf800000
	s_lshr_b32 s2, s30, 3
	s_lshl_b32 s2, s2, 7
	s_add_u32 s2, s2, 0x300000
	s_add_u32 s6, s6, s2
	s_addc_u32 s7, s7, 0
	s_mov_b32 s4, 0
	s_mov_b32 s5, 0x41d00000
	s_mov_b32 s16, 0
	s_mov_b32 s17, 0x420e0000
	s_waitcnt lgkmcnt(0)
	v_min3_f32 v2, v2, v3, v4
	v_min3_f32 v5, v5, v6, v7
	v_min3_f32 v2, v2, v10, v11
	v_min_f32_e32 v2, v2, v5
	s_waitcnt lgkmcnt(0)
	v_add_f32_e32 v20, v20, v21
	v_add_f32_e32 v22, v22, v23
	v_add_f32_e32 v24, v24, v25
	v_add_f32_e32 v26, v26, v27
	v_add_f32_e32 v28, v28, v29
	v_add_f32_e32 v30, v30, v31
	v_add_f32_e32 v32, v32, v33
	v_add_f32_e32 v34, v34, v35
	v_add_f32_e32 v20, v20, v22
	v_add_f32_e32 v24, v24, v26
	v_add_f32_e32 v28, v28, v30
	v_add_f32_e32 v32, v32, v34
	v_add_f32_e32 v20, v20, v24
	v_add_f32_e32 v28, v28, v32
	v_add_f32_e32 v20, v20, v28
	v_add_f32_e32 v2, v2, v20
	v_max_f32_e32 v2, 0, v2
	v_mul_f32_e32 v3, 0x4f800000, v2
	v_cmp_gt_f32_e32 vcc, s8, v2
	s_nop 1
	v_cndmask_b32_e32 v2, v2, v3, vcc
	v_sqrt_f32_e32 v3, v2
	s_nop 0
	v_add_u32_e32 v4, -1, v3
	v_fma_f32 v5, -v4, v3, v2
	v_cmp_ge_f32_e64 s[18:19], 0, v5
	v_add_u32_e32 v5, 1, v3
	s_nop 0
	v_cndmask_b32_e64 v4, v3, v4, s[18:19]
	v_fma_f32 v3, -v5, v3, v2
	v_cmp_lt_f32_e64 s[18:19], 0, v3
	s_nop 1
	v_cndmask_b32_e64 v3, v4, v5, s[18:19]
	v_mul_f32_e32 v4, 0x37800000, v3
	v_cndmask_b32_e32 v3, v3, v4, vcc
	v_mov_b32_e32 v4, 0x260
	v_cmp_class_f32_e32 vcc, v2, v4
	s_nop 1
	v_cndmask_b32_e32 v2, v3, v2, vcc
	s_nop 1
	v_add_f32_dpp v3, v2, v2 quad_perm:[1,0,3,2] row_mask:0xf bank_mask:0xf
	s_nop 1
	v_add_f32_dpp v4, v3, v3 quad_perm:[2,3,0,1] row_mask:0xf bank_mask:0xf
	s_nop 1
	v_add_f32_dpp v5, v4, v4 row_half_mirror row_mask:0xf bank_mask:0xf
	s_nop 1
	v_add_f32_dpp v6, v5, v5 row_mirror row_mask:0xf bank_mask:0xf
	s_nop 1
	v_readlane_b32 s12, v6, 0
	v_readlane_b32 s13, v6, 16
	v_readlane_b32 s14, v6, 32
	v_readlane_b32 s15, v6, 48
	s_nop 3
	v_mov_b32_e32 v7, s12
	v_add_f32_e32 v7, s13, v7
	v_mov_b32_e32 v9, s14
	v_add_f32_e32 v9, s15, v9
	v_add_f32_e32 v0, v7, v9
	v_mov_b32_e32 v4, 0
	s_mov_b64 exec, 1
	v_cvt_f64_f32_e32 v[6:7], v0
	v_add_f64 v[8:9], v[6:7], s[4:5]
	global_atomic_add_f64 v[10:11], v4, v[8:9], s[6:7] sc0
	s_waitcnt vmcnt(0)
	v_cmp_le_f64_e32 vcc, s[16:17], v[10:11]
	s_and_saveexec_b64 s[2:3], vcc
	s_cbranch_execz .Lmain_end
	v_add_f64 v[10:11], v[10:11], -s[16:17]
	v_add_f64 v[10:11], v[10:11], v[6:7]
	v_cvt_f32_f64_e32 v0, v[10:11]
	v_mul_f32_e32 v0, 0x38000000, v0
	global_atomic_add_f32 v4, v0, s[10:11]
